# dil_attn item loop header (both layers): counted vmcnt waits (4 dummy loads in the preheader) so the staged rows do not wait for the previous item's store acks
# speedup vs baseline: 1.0035x; 1.0010x over previous
.LBB0_1147:
	s_or_b64 exec, exec, s[8:9]
	s_add_u32 s4, s6, 0x3b600000
	s_addc_u32 s5, s7, 0
	s_add_u32 s6, s6, 0x3e600000
	s_addc_u32 s7, s7, 0
	s_bfe_u32 s2, s12, 0x20006
	s_mul_i32 s3, s50, 0xfc00
	s_add_i32 s3, s3, 0
	s_lshl_b32 s51, s90, 1
	s_lshl_b32 s26, s2, 4
	s_cmp_eq_u32 s2, 3
	s_cselect_b64 s[28:29], -1, 0
	s_cmp_gt_u32 s2, 1
	s_cselect_b64 s[30:31], -1, 0
	s_cmp_lg_u32 s2, 0
	v_and_b32_e32 v43, 63, v1
	s_cselect_b64 s[34:35], -1, 0
	s_cmp_lg_u32 s2, 3
	v_lshl_add_u32 v45, v42, 1, s3
	s_waitcnt vmcnt(6)
	v_and_b32_e32 v62, 48, v1
	v_mul_u32_u24_e32 v42, 0x90, v119
	v_lshrrev_b32_e32 v1, 2, v1
	v_lshlrev_b32_e32 v65, 2, v43
	s_cselect_b64 s[36:37], -1, 0
	s_cmp_lt_u32 s2, 2
	v_add3_u32 v63, s3, v42, v62
	v_and_b32_e32 v42, 12, v1
	v_xor_b32_e32 v1, 64, v65
	v_xor_b32_e32 v93, 0x80, v65
	v_and_b32_e32 v65, 24, v143
	s_cselect_b64 s[38:39], -1, 0
	s_cmp_eq_u32 s2, 0
	v_mov_b32_e32 v44, s3
	v_add_u32_e32 v65, s3, v65
	s_mul_i32 s3, s2, 0x900
	s_cselect_b64 s[40:41], -1, 0
	s_add_i32 s2, s26, 16
	s_waitcnt vmcnt(5)
	v_or3_b32 v66, s2, v142, v42
	s_add_i32 s2, s26, 32
	v_sub_u32_e32 v64, v42, v119
	v_or3_b32 v67, s2, v142, v42
	s_add_i32 s2, s26, 0x50
	v_or_b32_e32 v92, s26, v119
	v_cmp_lt_i32_e64 s[10:11], -1, v64
	v_cmp_lt_i32_e64 s[12:13], -2, v64
	v_cmp_lt_i32_e64 s[14:15], -3, v64
	v_cmp_lt_i32_e64 s[16:17], -4, v64
	v_cmp_gt_i32_e64 s[18:19], 1, v64
	v_cmp_gt_i32_e64 s[20:21], 0, v64
	v_cmp_gt_i32_e64 s[22:23], -1, v64
	v_cmp_gt_i32_e64 s[24:25], -2, v64
	v_or3_b32 v64, v142, s26, v42
	s_add_i32 s42, s26, 48
	v_add3_u32 v69, v142, s26, v42
	s_waitcnt vmcnt(4)
	v_or3_b32 v71, s2, v142, v42
	s_add_i32 s2, s26, 0x60
	s_addk_i32 s26, 0x70
	s_movk_i32 s8, 0x90
	v_or3_b32 v68, s42, v142, v42
	v_add_u32_e32 v70, 64, v69
	v_or3_b32 v72, s2, v142, v42
	v_or3_b32 v73, s26, v142, v42
	v_add_u32_e32 v69, 0x80, v69
	v_mad_u32_u24 v44, v92, s8, v44
	v_cmp_gt_u32_e64 s[8:9], 16, v43
	v_mul_u32_u24_e32 v43, 0x90, v86
	v_mul_u32_u24_e32 v64, 0x90, v64
	v_mul_u32_u24_e32 v66, 0x90, v66
	v_mul_u32_u24_e32 v67, 0x90, v67
	v_mul_u32_u24_e32 v68, 0x90, v68
	v_mul_u32_u24_e32 v70, 0x90, v70
	v_mul_u32_u24_e32 v71, 0x90, v71
	v_mul_u32_u24_e32 v72, 0x90, v72
	v_mul_u32_u24_e32 v73, 0x90, v73
	v_mul_u32_u24_e32 v69, 0x90, v69
	s_mov_b32 s27, 0
	s_add_i32 s52, s50, s51
	v_add_u32_e32 v94, v45, v43
	s_movk_i32 s53, 0x3400
	v_add_u32_e32 v95, v44, v62
	v_add_u32_e32 v96, s3, v63
	s_mov_b32 s54, 0xefa18f08
	v_add_u32_e32 v97, v65, v64
	v_add_u32_e32 v98, v65, v66
	v_add_u32_e32 v99, v65, v67
	v_add_u32_e32 v100, v65, v68
	v_add_u32_e32 v101, v65, v70
	v_add_u32_e32 v102, v65, v71
	v_add_u32_e32 v103, v65, v72
	v_add_u32_e32 v104, v65, v73
	v_add_u32_e32 v105, v65, v69
	v_lshlrev_b32_e32 v84, 1, v42
	v_mov_b32_e32 v42, 0
	v_mov_b32_e32 v106, 0xf149f2ca
	s_mov_b32 s26, s62
	v_mov_b32_e32 v150, 0
	global_load_dword v151, v150, s[4:5]
	global_load_dword v151, v150, s[4:5]
	global_load_dword v151, v150, s[4:5]
	global_load_dword v151, v150, s[4:5]
	s_branch .LBB0_1149

.LBB0_1149:
	s_waitcnt lgkmcnt(0)
	s_barrier
	s_waitcnt vmcnt(5)
	ds_write_b128 v94, v[2:5]
	s_waitcnt vmcnt(4)
	ds_write_b128 v94, v[6:9] offset:4608
	ds_write_b128 v94, v[14:17] offset:9216
	ds_write_b128 v94, v[18:21] offset:36864
	ds_write_b128 v94, v[10:13] offset:13824
	ds_write_b128 v94, v[22:25] offset:41472
	ds_write_b128 v94, v[26:29] offset:18432
	ds_write_b128 v94, v[30:33] offset:46080
	ds_write_b128 v94, v[34:37] offset:23040
	ds_write_b128 v94, v[38:41] offset:50688
	ds_write_b128 v94, v[46:49] offset:27648
	ds_write_b128 v94, v[50:53] offset:55296
	ds_write_b128 v94, v[54:57] offset:32256
	ds_write_b128 v94, v[58:61] offset:59904
	s_add_i32 s55, s26, s51
	s_waitcnt lgkmcnt(0)
	s_barrier
	s_cmpk_gt_i32 s55, 0x17ff
	s_cselect_b64 s[42:43], -1, 0
	s_and_b64 vcc, exec, s[42:43]
	s_cbranch_vccnz .LBB0_1163
	s_add_i32 s2, s52, s26
	s_and_b32 s3, s2, 63
	s_ashr_i32 s2, s2, 6
	s_mul_hi_i32 s44, s2, 0x55555556
	s_lshr_b32 s45, s44, 31
	s_add_i32 s44, s44, s45
	s_mul_i32 s45, s44, 3
	s_sub_i32 s2, s2, s45
	s_ashr_i32 s45, s44, 3
	s_cmp_eq_u32 s2, 1
	s_cselect_b32 s46, 2, 4
	s_cmp_lg_u32 s2, 0
	s_cselect_b32 s56, s46, 0
	s_lshr_b32 s2, 64, s56
	s_xor_b32 s46, s56, 6
	s_add_i32 s2, s2, -1
	s_lshr_b32 s57, s3, s46
	s_and_b32 s2, s2, s3
	s_mul_hi_i32 s3, s45, 0x3400000
	s_mul_i32 s45, s45, 0x3400000
	s_add_u32 s45, s0, s45
	s_addc_u32 s3, s1, s3
	s_lshl_b32 s44, s44, 7
	s_and_b32 s44, s44, 0x380
	s_add_u32 s44, s45, s44
	s_addc_u32 s3, s3, 0
	s_add_u32 s44, s44, 0x2800
	s_addc_u32 s45, s3, 0
	s_lshl_b32 s3, s2, 6
	v_or_b32_e32 v4, s3, v86
	v_or_b32_e32 v6, s3, v87
	v_lshlrev_b32_e32 v4, s56, v4
	v_lshlrev_b32_e32 v6, s56, v6
	v_lshl_add_u64 v[2:3], s[44:45], 0, v[82:83]
	v_add_u32_e32 v4, s57, v4
	v_add_u32_e32 v6, s57, v6
	v_mad_u64_u32 v[4:5], s[46:47], v4, s53, v[2:3]
	v_mad_u64_u32 v[6:7], s[46:47], v6, s53, v[2:3]
	global_load_dwordx4 v[2:5], v[4:5], off
	s_nop 0
	global_load_dwordx4 v[6:9], v[6:7], off
	s_lshr_b32 s58, 0x1000, s56
	s_sub_i32 s59, s3, 64
	v_or_b32_e32 v22, s59, v86
	s_cmp_lg_u32 s2, 0
	v_mov_b32_e32 v12, v42
	v_mov_b32_e32 v13, v42
	s_cselect_b64 s[46:47], -1, 0
	v_cmp_gt_i32_e32 vcc, s58, v22
	v_mov_b32_e32 v10, v42
	v_mov_b32_e32 v11, v42
	v_mov_b64_e32 v[16:17], v[12:13]
	v_mov_b64_e32 v[20:21], v[12:13]
	s_and_b64 s[60:61], s[46:47], vcc
	v_mov_b64_e32 v[14:15], v[10:11]
	v_mov_b64_e32 v[18:19], v[10:11]
	s_and_saveexec_b64 s[48:49], s[60:61]
	s_cbranch_execz .LBB0_1152
	v_lshlrev_b32_e32 v14, s56, v22
	v_add_u32_e32 v16, s57, v14
	v_mov_b64_e32 v[14:15], s[44:45]
	v_mad_u64_u32 v[14:15], s[60:61], v16, s53, v[14:15]
	v_lshl_add_u64 v[18:19], v[14:15], 0, v[82:83]
	global_load_dwordx4 v[14:17], v[18:19], off offset:1024
	s_nop 0
	global_load_dwordx4 v[18:21], v[18:19], off offset:2048

.LBB0_3465:
	s_or_b64 exec, exec, s[12:13]
	s_add_u32 s28, s4, 0x3b600000
	s_addc_u32 s29, s5, 0
	s_add_u32 s4, s4, 0x3e600000
	s_addc_u32 s5, s5, 0
	s_bfe_u32 s2, s9, 0x20006
	s_mul_i32 s3, s8, 0xfc00
	s_add_i32 s3, s3, 0
	s_lshl_b32 s9, s76, 1
	s_lshl_b32 s10, s2, 4
	s_cmp_eq_u32 s2, 3
	s_cselect_b64 s[34:35], -1, 0
	s_cmp_gt_u32 s2, 1
	s_cselect_b64 s[36:37], -1, 0
	s_cmp_lg_u32 s2, 0
	v_and_b32_e32 v43, 63, v1
	s_cselect_b64 s[38:39], -1, 0
	s_cmp_lg_u32 s2, 3
	v_lshl_add_u32 v45, v42, 1, s3
	s_waitcnt vmcnt(6)
	v_and_b32_e32 v62, 48, v1
	v_mul_u32_u24_e32 v42, 0x90, v142
	v_lshrrev_b32_e32 v1, 2, v1
	v_lshlrev_b32_e32 v65, 2, v43
	s_cselect_b64 s[40:41], -1, 0
	s_cmp_lt_u32 s2, 2
	v_add3_u32 v63, s3, v42, v62
	v_and_b32_e32 v42, 12, v1
	v_xor_b32_e32 v1, 64, v65
	v_xor_b32_e32 v93, 0x80, v65
	v_and_b32_e32 v65, 24, v144
	s_cselect_b64 s[42:43], -1, 0
	s_cmp_eq_u32 s2, 0
	v_mov_b32_e32 v44, s3
	v_add_u32_e32 v65, s3, v65
	s_mul_i32 s3, s2, 0x900
	s_cselect_b64 s[44:45], -1, 0
	s_add_i32 s2, s10, 16
	s_waitcnt vmcnt(5)
	v_or3_b32 v66, s2, v143, v42
	s_add_i32 s2, s10, 32
	v_sub_u32_e32 v64, v42, v142
	v_or3_b32 v67, s2, v143, v42
	s_add_i32 s2, s10, 0x50
	v_or_b32_e32 v92, s10, v142
	v_cmp_lt_i32_e64 s[12:13], -1, v64
	v_cmp_lt_i32_e64 s[14:15], -2, v64
	v_cmp_lt_i32_e64 s[16:17], -3, v64
	v_cmp_lt_i32_e64 s[18:19], -4, v64
	v_cmp_gt_i32_e64 s[20:21], 1, v64
	v_cmp_gt_i32_e64 s[22:23], 0, v64
	v_cmp_gt_i32_e64 s[24:25], -1, v64
	v_cmp_gt_i32_e64 s[26:27], -2, v64
	v_or3_b32 v64, v143, s10, v42
	s_add_i32 s11, s10, 48
	v_add3_u32 v69, v143, s10, v42
	s_waitcnt vmcnt(4)
	v_or3_b32 v71, s2, v143, v42
	s_add_i32 s2, s10, 0x60
	s_addk_i32 s10, 0x70
	s_movk_i32 s6, 0x90
	v_or3_b32 v68, s11, v143, v42
	v_add_u32_e32 v70, 64, v69
	v_or3_b32 v72, s2, v143, v42
	v_or3_b32 v73, s10, v143, v42
	v_add_u32_e32 v69, 0x80, v69
	v_mad_u32_u24 v44, v92, s6, v44
	v_cmp_gt_u32_e64 s[6:7], 16, v43
	v_mul_u32_u24_e32 v43, 0x90, v86
	v_mul_u32_u24_e32 v64, 0x90, v64
	v_mul_u32_u24_e32 v66, 0x90, v66
	v_mul_u32_u24_e32 v67, 0x90, v67
	v_mul_u32_u24_e32 v68, 0x90, v68
	v_mul_u32_u24_e32 v70, 0x90, v70
	v_mul_u32_u24_e32 v71, 0x90, v71
	v_mul_u32_u24_e32 v72, 0x90, v72
	v_mul_u32_u24_e32 v73, 0x90, v73
	v_mul_u32_u24_e32 v69, 0x90, v69
	s_mov_b32 s31, 0
	s_add_i32 s10, s8, s9
	v_add_u32_e32 v94, v45, v43
	s_movk_i32 s11, 0x3400
	v_add_u32_e32 v95, v44, v62
	v_add_u32_e32 v96, s3, v63
	s_mov_b32 s54, 0xefa18f08
	v_add_u32_e32 v97, v65, v64
	v_add_u32_e32 v98, v65, v66
	v_add_u32_e32 v99, v65, v67
	v_add_u32_e32 v100, v65, v68
	v_add_u32_e32 v101, v65, v70
	v_add_u32_e32 v102, v65, v71
	v_add_u32_e32 v103, v65, v72
	v_add_u32_e32 v104, v65, v73
	v_add_u32_e32 v105, v65, v69
	v_lshlrev_b32_e32 v84, 1, v42
	v_mov_b32_e32 v42, 0
	v_mov_b32_e32 v106, 0xf149f2ca
	s_mov_b32 s30, s60
	v_mov_b32_e32 v150, 0
	global_load_dword v151, v150, s[28:29]
	global_load_dword v151, v150, s[28:29]
	global_load_dword v151, v150, s[28:29]
	global_load_dword v151, v150, s[28:29]
	s_branch .LBB0_3467

.LBB0_3467:
	s_waitcnt lgkmcnt(0)
	s_barrier
	s_waitcnt vmcnt(5)
	ds_write_b128 v94, v[2:5]
	s_waitcnt vmcnt(4)
	ds_write_b128 v94, v[6:9] offset:4608
	ds_write_b128 v94, v[14:17] offset:9216
	ds_write_b128 v94, v[18:21] offset:36864
	ds_write_b128 v94, v[10:13] offset:13824
	ds_write_b128 v94, v[22:25] offset:41472
	ds_write_b128 v94, v[26:29] offset:18432
	ds_write_b128 v94, v[30:33] offset:46080
	ds_write_b128 v94, v[34:37] offset:23040
	ds_write_b128 v94, v[38:41] offset:50688
	ds_write_b128 v94, v[46:49] offset:27648
	ds_write_b128 v94, v[50:53] offset:55296
	ds_write_b128 v94, v[54:57] offset:32256
	ds_write_b128 v94, v[58:61] offset:59904
	s_add_i32 s55, s30, s9
	s_waitcnt lgkmcnt(0)
	s_barrier
	s_cmpk_gt_i32 s55, 0x17ff
	s_cselect_b64 s[46:47], -1, 0
	s_and_b64 vcc, exec, s[46:47]
	s_cbranch_vccnz .LBB0_3481
	s_add_i32 s2, s10, s30
	s_and_b32 s3, s2, 63
	s_ashr_i32 s2, s2, 6
	s_mul_hi_i32 s48, s2, 0x55555556
	s_lshr_b32 s49, s48, 31
	s_add_i32 s48, s48, s49
	s_mul_i32 s49, s48, 3
	s_sub_i32 s2, s2, s49
	s_ashr_i32 s49, s48, 3
	s_cmp_eq_u32 s2, 1
	s_cselect_b32 s50, 2, 4
	s_cmp_lg_u32 s2, 0
	s_cselect_b32 s56, s50, 0
	s_lshr_b32 s2, 64, s56
	s_xor_b32 s50, s56, 6
	s_add_i32 s2, s2, -1
	s_lshr_b32 s57, s3, s50
	s_and_b32 s50, s2, s3
	s_mul_hi_i32 s2, s49, 0x3400000
	s_mul_i32 s49, s49, 0x3400000
	s_add_u32 s3, s0, s49
	s_addc_u32 s2, s1, s2
	s_lshl_b32 s48, s48, 7
	s_and_b32 s48, s48, 0x380
	s_add_u32 s3, s3, s48
	s_addc_u32 s2, s2, 0
	s_add_u32 s48, s3, 0x2800
	s_addc_u32 s49, s2, 0
	s_lshl_b32 s51, s50, 6
	v_or_b32_e32 v4, s51, v86
	v_or_b32_e32 v6, s51, v87
	v_lshlrev_b32_e32 v4, s56, v4
	v_lshlrev_b32_e32 v6, s56, v6
	v_lshl_add_u64 v[2:3], s[48:49], 0, v[82:83]
	v_add_u32_e32 v4, s57, v4
	v_add_u32_e32 v6, s57, v6
	v_mad_u64_u32 v[4:5], s[2:3], v4, s11, v[2:3]
	v_mad_u64_u32 v[6:7], s[2:3], v6, s11, v[2:3]
	global_load_dwordx4 v[2:5], v[4:5], off
	s_nop 0
	global_load_dwordx4 v[6:9], v[6:7], off
	s_lshr_b32 s58, 0x1000, s56
	s_sub_i32 s59, s51, 64
	v_or_b32_e32 v22, s59, v86
	s_cmp_lg_u32 s50, 0
	v_mov_b32_e32 v12, v42
	v_mov_b32_e32 v13, v42
	s_cselect_b64 s[50:51], -1, 0
	v_cmp_gt_i32_e32 vcc, s58, v22
	v_mov_b32_e32 v10, v42
	v_mov_b32_e32 v11, v42
	v_mov_b64_e32 v[16:17], v[12:13]
	v_mov_b64_e32 v[20:21], v[12:13]
	s_and_b64 s[2:3], s[50:51], vcc
	v_mov_b64_e32 v[14:15], v[10:11]
	v_mov_b64_e32 v[18:19], v[10:11]
	s_and_saveexec_b64 s[52:53], s[2:3]
	s_cbranch_execz .LBB0_3470
	v_lshlrev_b32_e32 v14, s56, v22
	v_add_u32_e32 v16, s57, v14
	v_mov_b64_e32 v[14:15], s[48:49]
	v_mad_u64_u32 v[14:15], s[2:3], v16, s11, v[14:15]
	v_lshl_add_u64 v[18:19], v[14:15], 0, v[82:83]
	global_load_dwordx4 v[14:17], v[18:19], off offset:1024
	s_nop 0
	global_load_dwordx4 v[18:21], v[18:19], off offset:2048
